# gu fill_rowtab rewritten (geo table in lanes, scalar expert search, all 12 index loads in flight); dn reuses the geo table gu left in LDS
# speedup vs baseline: 1.0154x; 1.0038x over previous
.LBB0_1582:
	s_andn2_b64 vcc, exec, s[0:1]
	s_cbranch_vccnz .LBB0_1663
	s_mov_b64 s[0:1], exec
	v_readlane_b32 s4, v242, 30
	v_readlane_b32 s5, v242, 31
	s_and_b64 s[4:5], s[0:1], s[4:5]
	s_mov_b64 exec, s[4:5]
	s_cbranch_execz .LBB0_1633
	s_waitcnt vmcnt(0)
	v_and_b32_e32 v1, 63, v0
	v_min_u32_e32 v1, 16, v1
	v_lshlrev_b32_e32 v1, 2, v1
	v_add_u32_e32 v1, 0x20010, v1
	ds_read_b32 v14, v1
	ds_read_b32 v15, v1 offset:68
	v_readlane_b32 s4, v244, 55
	v_readlane_b32 s5, v244, 56
	v_readlane_b32 s10, v243, 52
	v_readlane_b32 s8, v243, 0
	s_ashr_i32 s9, s18, 3
	s_waitcnt lgkmcnt(0)
	v_readlane_b32 s6, v14, 16
	s_nop 3
	s_add_i32 s7, s6, 7
	s_ashr_i32 s7, s7, 3
	s_mul_i32 s8, s7, s8
	s_lshr_b32 s11, s10, 3
	s_add_i32 s12, s8, s11
	s_cmp_lt_i32 s11, s7
	s_cselect_b32 s13, s6, 0
	v_cmp_ge_i32_e32 vcc, s12, v14
	s_add_i32 s10, s10, s9
	s_nop 0
	s_and_b32 s100, vcc_lo, 0xfffe
	s_bcnt1_i32_b32 s100, s100
	s_cmp_lt_i32 s12, s13
	s_nop 3
	v_readlane_b32 s101, v14, s100
	v_readlane_b32 s13, v15, s100
	s_nop 3
	s_cselect_b32 s13, s13, 0
	s_sub_i32 s101, s12, s101
	s_lshl_b32 s101, s101, 8
	s_lshl_b32 s100, s100, 17
	s_add_i32 s100, s100, 0x151000
	v_add_u32_e32 v13, s101, v0
	v_cmp_gt_i32_e32 vcc, s13, v13
	v_lshl_add_u32 v1, v13, 2, s100
	s_nop 1
	v_cndmask_b32_e32 v1, 0, v1, vcc
	global_load_dword v1, v1, s[4:5]
	s_lshr_b32 s11, s10, 3
	s_add_i32 s12, s8, s11
	s_cmp_lt_i32 s11, s7
	s_cselect_b32 s13, s6, 0
	v_cmp_ge_i32_e32 vcc, s12, v14
	s_add_i32 s10, s10, s9
	s_nop 0
	s_and_b32 s100, vcc_lo, 0xfffe
	s_bcnt1_i32_b32 s100, s100
	s_cmp_lt_i32 s12, s13
	s_nop 3
	v_readlane_b32 s101, v14, s100
	v_readlane_b32 s13, v15, s100
	s_nop 3
	s_cselect_b32 s13, s13, 0
	s_sub_i32 s101, s12, s101
	s_lshl_b32 s101, s101, 8
	s_lshl_b32 s100, s100, 17
	s_add_i32 s100, s100, 0x151000
	v_add_u32_e32 v13, s101, v0
	v_cmp_gt_i32_e32 vcc, s13, v13
	v_lshl_add_u32 v2, v13, 2, s100
	s_nop 1
	v_cndmask_b32_e32 v2, 0, v2, vcc
	global_load_dword v2, v2, s[4:5]
	s_lshr_b32 s11, s10, 3
	s_add_i32 s12, s8, s11
	s_cmp_lt_i32 s11, s7
	s_cselect_b32 s13, s6, 0
	v_cmp_ge_i32_e32 vcc, s12, v14
	s_add_i32 s10, s10, s9
	s_nop 0
	s_and_b32 s100, vcc_lo, 0xfffe
	s_bcnt1_i32_b32 s100, s100
	s_cmp_lt_i32 s12, s13
	s_nop 3
	v_readlane_b32 s101, v14, s100
	v_readlane_b32 s13, v15, s100
	s_nop 3
	s_cselect_b32 s13, s13, 0
	s_sub_i32 s101, s12, s101
	s_lshl_b32 s101, s101, 8
	s_lshl_b32 s100, s100, 17
	s_add_i32 s100, s100, 0x151000
	v_add_u32_e32 v13, s101, v0
	v_cmp_gt_i32_e32 vcc, s13, v13
	v_lshl_add_u32 v3, v13, 2, s100
	s_nop 1
	v_cndmask_b32_e32 v3, 0, v3, vcc
	global_load_dword v3, v3, s[4:5]
	s_lshr_b32 s11, s10, 3
	s_add_i32 s12, s8, s11
	s_cmp_lt_i32 s11, s7
	s_cselect_b32 s13, s6, 0
	v_cmp_ge_i32_e32 vcc, s12, v14
	s_add_i32 s10, s10, s9
	s_nop 0
	s_and_b32 s100, vcc_lo, 0xfffe
	s_bcnt1_i32_b32 s100, s100
	s_cmp_lt_i32 s12, s13
	s_nop 3
	v_readlane_b32 s101, v14, s100
	v_readlane_b32 s13, v15, s100
	s_nop 3
	s_cselect_b32 s13, s13, 0
	s_sub_i32 s101, s12, s101
	s_lshl_b32 s101, s101, 8
	s_lshl_b32 s100, s100, 17
	s_add_i32 s100, s100, 0x151000
	v_add_u32_e32 v13, s101, v0
	v_cmp_gt_i32_e32 vcc, s13, v13
	v_lshl_add_u32 v4, v13, 2, s100
	s_nop 1
	v_cndmask_b32_e32 v4, 0, v4, vcc
	global_load_dword v4, v4, s[4:5]
	s_lshr_b32 s11, s10, 3
	s_add_i32 s12, s8, s11
	s_cmp_lt_i32 s11, s7
	s_cselect_b32 s13, s6, 0
	v_cmp_ge_i32_e32 vcc, s12, v14
	s_add_i32 s10, s10, s9
	s_nop 0
	s_and_b32 s100, vcc_lo, 0xfffe
	s_bcnt1_i32_b32 s100, s100
	s_cmp_lt_i32 s12, s13
	s_nop 3
	v_readlane_b32 s101, v14, s100
	v_readlane_b32 s13, v15, s100
	s_nop 3
	s_cselect_b32 s13, s13, 0
	s_sub_i32 s101, s12, s101
	s_lshl_b32 s101, s101, 8
	s_lshl_b32 s100, s100, 17
	s_add_i32 s100, s100, 0x151000
	v_add_u32_e32 v13, s101, v0
	v_cmp_gt_i32_e32 vcc, s13, v13
	v_lshl_add_u32 v5, v13, 2, s100
	s_nop 1
	v_cndmask_b32_e32 v5, 0, v5, vcc
	global_load_dword v5, v5, s[4:5]
	s_lshr_b32 s11, s10, 3
	s_add_i32 s12, s8, s11
	s_cmp_lt_i32 s11, s7
	s_cselect_b32 s13, s6, 0
	v_cmp_ge_i32_e32 vcc, s12, v14
	s_add_i32 s10, s10, s9
	s_nop 0
	s_and_b32 s100, vcc_lo, 0xfffe
	s_bcnt1_i32_b32 s100, s100
	s_cmp_lt_i32 s12, s13
	s_nop 3
	v_readlane_b32 s101, v14, s100
	v_readlane_b32 s13, v15, s100
	s_nop 3
	s_cselect_b32 s13, s13, 0
	s_sub_i32 s101, s12, s101
	s_lshl_b32 s101, s101, 8
	s_lshl_b32 s100, s100, 17
	s_add_i32 s100, s100, 0x151000
	v_add_u32_e32 v13, s101, v0
	v_cmp_gt_i32_e32 vcc, s13, v13
	v_lshl_add_u32 v6, v13, 2, s100
	s_nop 1
	v_cndmask_b32_e32 v6, 0, v6, vcc
	global_load_dword v6, v6, s[4:5]
	s_lshr_b32 s11, s10, 3
	s_add_i32 s12, s8, s11
	s_cmp_lt_i32 s11, s7
	s_cselect_b32 s13, s6, 0
	v_cmp_ge_i32_e32 vcc, s12, v14
	s_add_i32 s10, s10, s9
	s_nop 0
	s_and_b32 s100, vcc_lo, 0xfffe
	s_bcnt1_i32_b32 s100, s100
	s_cmp_lt_i32 s12, s13
	s_nop 3
	v_readlane_b32 s101, v14, s100
	v_readlane_b32 s13, v15, s100
	s_nop 3
	s_cselect_b32 s13, s13, 0
	s_sub_i32 s101, s12, s101
	s_lshl_b32 s101, s101, 8
	s_lshl_b32 s100, s100, 17
	s_add_i32 s100, s100, 0x151000
	v_add_u32_e32 v13, s101, v0
	v_cmp_gt_i32_e32 vcc, s13, v13
	v_lshl_add_u32 v7, v13, 2, s100
	s_nop 1
	v_cndmask_b32_e32 v7, 0, v7, vcc
	global_load_dword v7, v7, s[4:5]
	s_lshr_b32 s11, s10, 3
	s_add_i32 s12, s8, s11
	s_cmp_lt_i32 s11, s7
	s_cselect_b32 s13, s6, 0
	v_cmp_ge_i32_e32 vcc, s12, v14
	s_add_i32 s10, s10, s9
	s_nop 0
	s_and_b32 s100, vcc_lo, 0xfffe
	s_bcnt1_i32_b32 s100, s100
	s_cmp_lt_i32 s12, s13
	s_nop 3
	v_readlane_b32 s101, v14, s100
	v_readlane_b32 s13, v15, s100
	s_nop 3
	s_cselect_b32 s13, s13, 0
	s_sub_i32 s101, s12, s101
	s_lshl_b32 s101, s101, 8
	s_lshl_b32 s100, s100, 17
	s_add_i32 s100, s100, 0x151000
	v_add_u32_e32 v13, s101, v0
	v_cmp_gt_i32_e32 vcc, s13, v13
	v_lshl_add_u32 v8, v13, 2, s100
	s_nop 1
	v_cndmask_b32_e32 v8, 0, v8, vcc
	global_load_dword v8, v8, s[4:5]
	s_lshr_b32 s11, s10, 3
	s_add_i32 s12, s8, s11
	s_cmp_lt_i32 s11, s7
	s_cselect_b32 s13, s6, 0
	v_cmp_ge_i32_e32 vcc, s12, v14
	s_add_i32 s10, s10, s9
	s_nop 0
	s_and_b32 s100, vcc_lo, 0xfffe
	s_bcnt1_i32_b32 s100, s100
	s_cmp_lt_i32 s12, s13
	s_nop 3
	v_readlane_b32 s101, v14, s100
	v_readlane_b32 s13, v15, s100
	s_nop 3
	s_cselect_b32 s13, s13, 0
	s_sub_i32 s101, s12, s101
	s_lshl_b32 s101, s101, 8
	s_lshl_b32 s100, s100, 17
	s_add_i32 s100, s100, 0x151000
	v_add_u32_e32 v13, s101, v0
	v_cmp_gt_i32_e32 vcc, s13, v13
	v_lshl_add_u32 v9, v13, 2, s100
	s_nop 1
	v_cndmask_b32_e32 v9, 0, v9, vcc
	global_load_dword v9, v9, s[4:5]
	s_lshr_b32 s11, s10, 3
	s_add_i32 s12, s8, s11
	s_cmp_lt_i32 s11, s7
	s_cselect_b32 s13, s6, 0
	v_cmp_ge_i32_e32 vcc, s12, v14
	s_add_i32 s10, s10, s9
	s_nop 0
	s_and_b32 s100, vcc_lo, 0xfffe
	s_bcnt1_i32_b32 s100, s100
	s_cmp_lt_i32 s12, s13
	s_nop 3
	v_readlane_b32 s101, v14, s100
	v_readlane_b32 s13, v15, s100
	s_nop 3
	s_cselect_b32 s13, s13, 0
	s_sub_i32 s101, s12, s101
	s_lshl_b32 s101, s101, 8
	s_lshl_b32 s100, s100, 17
	s_add_i32 s100, s100, 0x151000
	v_add_u32_e32 v13, s101, v0
	v_cmp_gt_i32_e32 vcc, s13, v13
	v_lshl_add_u32 v10, v13, 2, s100
	s_nop 1
	v_cndmask_b32_e32 v10, 0, v10, vcc
	global_load_dword v10, v10, s[4:5]
	s_lshr_b32 s11, s10, 3
	s_add_i32 s12, s8, s11
	s_cmp_lt_i32 s11, s7
	s_cselect_b32 s13, s6, 0
	v_cmp_ge_i32_e32 vcc, s12, v14
	s_add_i32 s10, s10, s9
	s_nop 0
	s_and_b32 s100, vcc_lo, 0xfffe
	s_bcnt1_i32_b32 s100, s100
	s_cmp_lt_i32 s12, s13
	s_nop 3
	v_readlane_b32 s101, v14, s100
	v_readlane_b32 s13, v15, s100
	s_nop 3
	s_cselect_b32 s13, s13, 0
	s_sub_i32 s101, s12, s101
	s_lshl_b32 s101, s101, 8
	s_lshl_b32 s100, s100, 17
	s_add_i32 s100, s100, 0x151000
	v_add_u32_e32 v13, s101, v0
	v_cmp_gt_i32_e32 vcc, s13, v13
	v_lshl_add_u32 v11, v13, 2, s100
	s_nop 1
	v_cndmask_b32_e32 v11, 0, v11, vcc
	global_load_dword v11, v11, s[4:5]
	s_lshr_b32 s11, s10, 3
	s_add_i32 s12, s8, s11
	s_cmp_lt_i32 s11, s7
	s_cselect_b32 s13, s6, 0
	v_cmp_ge_i32_e32 vcc, s12, v14
	s_add_i32 s10, s10, s9
	s_nop 0
	s_and_b32 s100, vcc_lo, 0xfffe
	s_bcnt1_i32_b32 s100, s100
	s_cmp_lt_i32 s12, s13
	s_nop 3
	v_readlane_b32 s101, v14, s100
	v_readlane_b32 s13, v15, s100
	s_nop 3
	s_cselect_b32 s13, s13, 0
	s_sub_i32 s101, s12, s101
	s_lshl_b32 s101, s101, 8
	s_lshl_b32 s100, s100, 17
	s_add_i32 s100, s100, 0x151000
	v_add_u32_e32 v13, s101, v0
	v_cmp_gt_i32_e32 vcc, s13, v13
	v_lshl_add_u32 v12, v13, 2, s100
	s_nop 1
	v_cndmask_b32_e32 v12, 0, v12, vcc
	global_load_dword v12, v12, s[4:5]
	s_waitcnt vmcnt(0)
	v_lshlrev_b32_e32 v1, 9, v1
	v_lshlrev_b32_e32 v2, 9, v2
	v_lshlrev_b32_e32 v3, 9, v3
	v_lshlrev_b32_e32 v4, 9, v4
	v_lshlrev_b32_e32 v5, 9, v5
	v_lshlrev_b32_e32 v6, 9, v6
	v_lshlrev_b32_e32 v7, 9, v7
	v_lshlrev_b32_e32 v8, 9, v8
	v_lshlrev_b32_e32 v9, 9, v9
	v_lshlrev_b32_e32 v10, 9, v10
	v_lshlrev_b32_e32 v11, 9, v11
	v_lshlrev_b32_e32 v12, 9, v12
	v_and_b32_e32 v1, 0xfffffc00, v1
	v_and_b32_e32 v2, 0xfffffc00, v2
	v_and_b32_e32 v3, 0xfffffc00, v3
	v_and_b32_e32 v4, 0xfffffc00, v4
	v_and_b32_e32 v5, 0xfffffc00, v5
	v_and_b32_e32 v6, 0xfffffc00, v6
	v_and_b32_e32 v7, 0xfffffc00, v7
	v_and_b32_e32 v8, 0xfffffc00, v8
	v_and_b32_e32 v9, 0xfffffc00, v9
	v_and_b32_e32 v10, 0xfffffc00, v10
	v_and_b32_e32 v11, 0xfffffc00, v11
	v_and_b32_e32 v12, 0xfffffc00, v12
	ds_write2st64_b32 v200, v1, v2 offset1:4
	ds_write2st64_b32 v200, v3, v4 offset0:8 offset1:12
	ds_write2st64_b32 v200, v5, v6 offset0:16 offset1:20
	ds_write2st64_b32 v200, v7, v8 offset0:24 offset1:28
	ds_write2st64_b32 v200, v9, v10 offset0:32 offset1:36
	ds_write2st64_b32 v200, v11, v12 offset0:40 offset1:44

.LBB0_1718:
	s_mov_b64 s[0:1], exec
	v_readlane_b32 s4, v244, 35
	v_readlane_b32 s5, v244, 36
	v_readlane_b32 s56, v246, 15
	v_readlane_b32 s26, v243, 57
	s_and_b64 s[4:5], s[0:1], s[4:5]
	v_readlane_b32 s57, v246, 16
	v_readlane_b32 s27, v243, 58
	s_mov_b64 exec, s[4:5]
	s_branch .LBB0_1725
	v_mov_b32_e32 v1, 0
	s_mov_b64 s[4:5], exec
	v_readlane_b32 s6, v244, 37
	v_readlane_b32 s7, v244, 38
	s_and_b64 s[6:7], s[4:5], s[6:7]
	s_mov_b64 exec, s[6:7]
	s_cbranch_execz .LBB0_1721
	v_readlane_b32 s6, v244, 22
	s_nop 1
	v_lshl_or_b32 v194, s6, 10, v199
	v_readlane_b32 s6, v243, 40
	v_readlane_b32 s7, v243, 41
	s_waitcnt vmcnt(7)
	s_nop 0
	v_lshl_add_u64 v[2:3], v[194:195], 2, s[6:7]
	global_load_dword v1, v[2:3], off sc1

	.amdhsa_kernel _Z4mega1Pii
		.amdhsa_group_segment_fixed_size 0
		.amdhsa_private_segment_fixed_size 0
		.amdhsa_kernarg_size 480
		.amdhsa_user_sgpr_count 2
		.amdhsa_user_sgpr_dispatch_ptr 0
		.amdhsa_user_sgpr_queue_ptr 0
		.amdhsa_user_sgpr_kernarg_segment_ptr 1
		.amdhsa_user_sgpr_dispatch_id 0
		.amdhsa_user_sgpr_kernarg_preload_length 0
		.amdhsa_user_sgpr_kernarg_preload_offset 0
		.amdhsa_user_sgpr_private_segment_size 0
		.amdhsa_uses_dynamic_stack 0
		.amdhsa_enable_private_segment 0
		.amdhsa_system_sgpr_workgroup_id_x 1
		.amdhsa_system_sgpr_workgroup_id_y 0
		.amdhsa_system_sgpr_workgroup_id_z 0
		.amdhsa_system_sgpr_workgroup_info 0
		.amdhsa_system_vgpr_workitem_id 0
		.amdhsa_next_free_vgpr 252
		.amdhsa_next_free_sgpr 102
		.amdhsa_accum_offset 252
		.amdhsa_reserve_vcc 1
		.amdhsa_float_round_mode_32 0
		.amdhsa_float_round_mode_16_64 0
		.amdhsa_float_denorm_mode_32 3
		.amdhsa_float_denorm_mode_16_64 3
		.amdhsa_dx10_clamp 1
		.amdhsa_ieee_mode 1
		.amdhsa_fp16_overflow 0
		.amdhsa_tg_split 0
		.amdhsa_exception_fp_ieee_invalid_op 0
		.amdhsa_exception_fp_denorm_src 0
		.amdhsa_exception_fp_ieee_div_zero 0
		.amdhsa_exception_fp_ieee_overflow 0
		.amdhsa_exception_fp_ieee_underflow 0
		.amdhsa_exception_fp_ieee_inexact 0
		.amdhsa_exception_int_div_zero 0
	.end_amdhsa_kernel

amdhsa.kernels:
  - .agpr_count:     0
    .args:
      - .offset:         0
        .size:           216
        .value_kind:     by_value
      - .offset:         216
        .size:           4
        .value_kind:     by_value
      - .offset:         220
        .size:           4
        .value_kind:     by_value
      - .offset:         224
        .size:           4
        .value_kind:     hidden_block_count_x
      - .offset:         228
        .size:           4
        .value_kind:     hidden_block_count_y
      - .offset:         232
        .size:           4
        .value_kind:     hidden_block_count_z
      - .offset:         236
        .size:           2
        .value_kind:     hidden_group_size_x
      - .offset:         238
        .size:           2
        .value_kind:     hidden_group_size_y
      - .offset:         240
        .size:           2
        .value_kind:     hidden_group_size_z
      - .offset:         242
        .size:           2
        .value_kind:     hidden_remainder_x
      - .offset:         244
        .size:           2
        .value_kind:     hidden_remainder_y
      - .offset:         246
        .size:           2
        .value_kind:     hidden_remainder_z
      - .offset:         264
        .size:           8
        .value_kind:     hidden_global_offset_x
      - .offset:         272
        .size:           8
        .value_kind:     hidden_global_offset_y
      - .offset:         280
        .size:           8
        .value_kind:     hidden_global_offset_z
      - .offset:         288
        .size:           2
        .value_kind:     hidden_grid_dims
      - .offset:         344
        .size:           4
        .value_kind:     hidden_dynamic_lds_size
    .group_segment_fixed_size: 0
    .kernarg_segment_align: 8
    .kernarg_segment_size: 480
    .language:       OpenCL C
    .language_version:
      - 2
      - 0
    .max_flat_workgroup_size: 512
    .name:           _Z4mega1Pii
    .private_segment_fixed_size: 0
    .sgpr_count:     108
    .sgpr_spill_count: 438
    .symbol:         _Z4mega1Pii.kd
    .uniform_work_group_size: 1
    .uses_dynamic_stack: false
    .vgpr_count:     252
    .vgpr_spill_count: 0
    .wavefront_size: 64
